# speedup vs baseline: 1.0268x; 1.0268x over previous
_Z11main_kernelPKcPfS1_:
	s_load_dwordx2 s[6:7], s[0:1], 0x0
	s_and_b32 s3, s2, 7
	s_lshr_b32 s4, s2, 3
	s_and_b32 s5, s4, 3
	s_lshl_b32 s3, s3, 2
	s_or_b32 s8, s3, s5
	s_lshr_b32 s9, s4, 2
	v_lshrrev_b32_e32 v127, 6, v0
	v_and_b32_e32 v124, 63, v0
	v_lshlrev_b32_e32 v124, 4, v124
	v_mov_b32_e32 v120, 0
	v_readfirstlane_b32 s12, v127
	v_mov_b32_e32 v121, 0
	v_mov_b32_e32 v122, 0
	v_mov_b32_e32 v123, 0
	s_lshl_b32 s13, s12, 10
	s_lshl_b32 s14, s9, 3
	s_add_u32 s14, s14, s12
	s_lshl_b32 s15, s14, 13
	s_mul_i32 s16, s8, 0x18000
	s_add_u32 s16, s16, 0x100000
	v_or_b32_e32 v125, s13, v124
	v_or_b32_e32 v126, 0x2000, v125
	s_add_u32 s20, s13, 0x2000
	s_waitcnt lgkmcnt(0)
	s_add_u32 s10, s6, s16
	s_addc_u32 s11, s7, 0
	s_add_u32 s18, s6, s15
	s_addc_u32 s19, s7, 0
	s_add_u32 s22, s18, 0x1000
	s_addc_u32 s23, s19, 0
	s_mov_b32 m0, s13
	s_nop 0
	global_load_lds_dwordx4 v125, s[10:11]
	s_mov_b32 m0, s20
	s_nop 0
	global_load_lds_dwordx4 v126, s[10:11]
	global_load_dwordx4 v[96:99], v124, s[18:19]
	global_load_dwordx2 v[100:101], v124, s[18:19] offset:1024
	global_load_dwordx4 v[102:105], v124, s[18:19] offset:2048
	global_load_dwordx2 v[106:107], v124, s[18:19] offset:3072
	global_load_dwordx4 v[108:111], v124, s[22:23]
	global_load_dwordx2 v[112:113], v124, s[22:23] offset:1024
	global_load_dwordx4 v[114:117], v124, s[22:23] offset:2048
	global_load_dwordx2 v[118:119], v124, s[22:23] offset:3072
	s_add_u32 s24, s10, 0x4000
	s_addc_u32 s25, s11, 0
	s_add_u32 s26, s13, 0x4000
	s_mov_b32 m0, s26
	s_nop 0
	global_load_lds_dwordx4 v125, s[24:25]
	s_add_u32 s26, s20, 0x4000
	s_mov_b32 m0, s26
	s_nop 0
	global_load_lds_dwordx4 v126, s[24:25]
	s_add_u32 s24, s10, 0x8000
	s_addc_u32 s25, s11, 0
	s_add_u32 s26, s13, 0x8000
	s_mov_b32 m0, s26
	s_nop 0
	global_load_lds_dwordx4 v125, s[24:25]
	s_add_u32 s26, s20, 0x8000
	s_mov_b32 m0, s26
	s_nop 0
	global_load_lds_dwordx4 v126, s[24:25]
	s_add_u32 s24, s10, 0xc000
	s_addc_u32 s25, s11, 0
	s_add_u32 s26, s13, 0xc000
	s_mov_b32 m0, s26
	s_nop 0
	global_load_lds_dwordx4 v125, s[24:25]
	s_add_u32 s26, s20, 0xc000
	s_mov_b32 m0, s26
	s_nop 0
	global_load_lds_dwordx4 v126, s[24:25]
	s_waitcnt vmcnt(6)
	s_barrier
	ds_read_b128 v[0:3], v124
	ds_read_b64 v[4:5], v124 offset:1024
	ds_read_b128 v[6:9], v124 offset:2048
	ds_read_b64 v[10:11], v124 offset:3072
	ds_read_b128 v[12:15], v124 offset:4096
	ds_read_b64 v[16:17], v124 offset:5120
	ds_read_b128 v[18:21], v124 offset:6144
	ds_read_b64 v[22:23], v124 offset:7168
	ds_read_b128 v[24:27], v124 offset:8192
	ds_read_b64 v[28:29], v124 offset:9216
	ds_read_b128 v[30:33], v124 offset:10240
	ds_read_b64 v[34:35], v124 offset:11264
	ds_read_b128 v[36:39], v124 offset:12288
	ds_read_b64 v[40:41], v124 offset:13312
	ds_read_b128 v[42:45], v124 offset:14336
	ds_read_b64 v[46:47], v124 offset:15360
	s_waitcnt vmcnt(4) lgkmcnt(0)
	s_barrier
	s_add_u32 s24, s10, 0x10000
	s_addc_u32 s25, s11, 0
	s_mov_b32 m0, s13
	s_nop 0
	global_load_lds_dwordx4 v125, s[24:25]
	s_mov_b32 m0, s20
	s_nop 0
	global_load_lds_dwordx4 v126, s[24:25]
	s_setprio 3
	v_mfma_f32_32x32x64_f8f6f4 v[48:63], v[0:5], v[96:101], 0 cbsz:2 blgp:2
	ds_read_b128 v[0:3], v124 offset:16384
	ds_read_b64 v[4:5], v124 offset:17408
	v_mfma_f32_32x32x64_f8f6f4 v[48:63], v[6:11], v[102:107], v[48:63] cbsz:2 blgp:2
	ds_read_b128 v[6:9], v124 offset:18432
	ds_read_b64 v[10:11], v124 offset:19456
	v_mfma_f32_32x32x64_f8f6f4 v[48:63], v[12:17], v[108:113], v[48:63] cbsz:2 blgp:2
	ds_read_b128 v[12:15], v124 offset:20480
	ds_read_b64 v[16:17], v124 offset:21504
	v_mfma_f32_32x32x64_f8f6f4 v[48:63], v[18:23], v[114:119], v[48:63] cbsz:2 blgp:2
	ds_read_b128 v[18:21], v124 offset:22528
	ds_read_b64 v[22:23], v124 offset:23552
	s_waitcnt lgkmcnt(8)
	v_mfma_f32_32x32x64_f8f6f4 v[64:79], v[24:29], v[96:101], 0 cbsz:2 blgp:2
	ds_read_b128 v[24:27], v124 offset:24576
	ds_read_b64 v[28:29], v124 offset:25600
	v_mfma_f32_32x32x64_f8f6f4 v[64:79], v[30:35], v[102:107], v[64:79] cbsz:2 blgp:2
	ds_read_b128 v[30:33], v124 offset:26624
	ds_read_b64 v[34:35], v124 offset:27648
	s_nop 4
	v_exp_f32_e32 v48, v48
	v_exp_f32_e32 v49, v49
	v_exp_f32_e32 v50, v50
	v_exp_f32_e32 v51, v51
	v_pk_add_f32 v[120:121], v[120:121], v[48:49]
	v_pk_add_f32 v[122:123], v[122:123], v[50:51]
	v_mfma_f32_32x32x64_f8f6f4 v[64:79], v[36:41], v[108:113], v[64:79] cbsz:2 blgp:2
	ds_read_b128 v[36:39], v124 offset:28672
	ds_read_b64 v[40:41], v124 offset:29696
	v_exp_f32_e32 v52, v52
	v_exp_f32_e32 v53, v53
	v_exp_f32_e32 v54, v54
	v_exp_f32_e32 v55, v55
	v_pk_add_f32 v[120:121], v[120:121], v[52:53]
	v_pk_add_f32 v[122:123], v[122:123], v[54:55]
	v_mfma_f32_32x32x64_f8f6f4 v[64:79], v[42:47], v[114:119], v[64:79] cbsz:2 blgp:2
	ds_read_b128 v[42:45], v124 offset:30720
	ds_read_b64 v[46:47], v124 offset:31744
	v_exp_f32_e32 v56, v56
	v_exp_f32_e32 v57, v57
	v_exp_f32_e32 v58, v58
	v_exp_f32_e32 v59, v59
	v_pk_add_f32 v[120:121], v[120:121], v[56:57]
	v_pk_add_f32 v[122:123], v[122:123], v[58:59]
	s_waitcnt vmcnt(4) lgkmcnt(0)
	s_barrier
	s_add_u32 s24, s10, 0x14000
	s_addc_u32 s25, s11, 0
	s_add_u32 s26, s13, 0x4000
	s_mov_b32 m0, s26
	s_nop 0
	global_load_lds_dwordx4 v125, s[24:25]
	s_add_u32 s26, s20, 0x4000
	s_mov_b32 m0, s26
	s_nop 0
	global_load_lds_dwordx4 v126, s[24:25]
	v_mfma_f32_32x32x64_f8f6f4 v[80:95], v[0:5], v[96:101], 0 cbsz:2 blgp:2
	ds_read_b128 v[0:3], v124 offset:32768
	ds_read_b64 v[4:5], v124 offset:33792
	v_exp_f32_e32 v60, v60
	v_exp_f32_e32 v61, v61
	v_exp_f32_e32 v62, v62
	v_exp_f32_e32 v63, v63
	v_pk_add_f32 v[120:121], v[120:121], v[60:61]
	v_pk_add_f32 v[122:123], v[122:123], v[62:63]
	v_mfma_f32_32x32x64_f8f6f4 v[80:95], v[6:11], v[102:107], v[80:95] cbsz:2 blgp:2
	ds_read_b128 v[6:9], v124 offset:34816
	ds_read_b64 v[10:11], v124 offset:35840
	v_exp_f32_e32 v64, v64
	v_exp_f32_e32 v65, v65
	v_exp_f32_e32 v66, v66
	v_exp_f32_e32 v67, v67
	v_pk_add_f32 v[120:121], v[120:121], v[64:65]
	v_pk_add_f32 v[122:123], v[122:123], v[66:67]
	v_mfma_f32_32x32x64_f8f6f4 v[80:95], v[12:17], v[108:113], v[80:95] cbsz:2 blgp:2
	ds_read_b128 v[12:15], v124 offset:36864
	ds_read_b64 v[16:17], v124 offset:37888
	v_exp_f32_e32 v68, v68
	v_exp_f32_e32 v69, v69
	v_exp_f32_e32 v70, v70
	v_exp_f32_e32 v71, v71
	v_pk_add_f32 v[120:121], v[120:121], v[68:69]
	v_pk_add_f32 v[122:123], v[122:123], v[70:71]
	v_mfma_f32_32x32x64_f8f6f4 v[80:95], v[18:23], v[114:119], v[80:95] cbsz:2 blgp:2
	ds_read_b128 v[18:21], v124 offset:38912
	ds_read_b64 v[22:23], v124 offset:39936
	v_exp_f32_e32 v72, v72
	v_exp_f32_e32 v73, v73
	v_exp_f32_e32 v74, v74
	v_exp_f32_e32 v75, v75
	v_pk_add_f32 v[120:121], v[120:121], v[72:73]
	v_pk_add_f32 v[122:123], v[122:123], v[74:75]
	s_waitcnt lgkmcnt(8)
	v_mfma_f32_32x32x64_f8f6f4 v[48:63], v[24:29], v[96:101], 0 cbsz:2 blgp:2
	ds_read_b128 v[24:27], v124 offset:40960
	ds_read_b64 v[28:29], v124 offset:41984
	v_exp_f32_e32 v76, v76
	v_exp_f32_e32 v77, v77
	v_exp_f32_e32 v78, v78
	v_exp_f32_e32 v79, v79
	v_pk_add_f32 v[120:121], v[120:121], v[76:77]
	v_pk_add_f32 v[122:123], v[122:123], v[78:79]
	v_mfma_f32_32x32x64_f8f6f4 v[48:63], v[30:35], v[102:107], v[48:63] cbsz:2 blgp:2
	ds_read_b128 v[30:33], v124 offset:43008
	ds_read_b64 v[34:35], v124 offset:44032
	v_exp_f32_e32 v80, v80
	v_exp_f32_e32 v81, v81
	v_exp_f32_e32 v82, v82
	v_exp_f32_e32 v83, v83
	v_pk_add_f32 v[120:121], v[120:121], v[80:81]
	v_pk_add_f32 v[122:123], v[122:123], v[82:83]
	v_mfma_f32_32x32x64_f8f6f4 v[48:63], v[36:41], v[108:113], v[48:63] cbsz:2 blgp:2
	ds_read_b128 v[36:39], v124 offset:45056
	ds_read_b64 v[40:41], v124 offset:46080
	v_exp_f32_e32 v84, v84
	v_exp_f32_e32 v85, v85
	v_exp_f32_e32 v86, v86
	v_exp_f32_e32 v87, v87
	v_pk_add_f32 v[120:121], v[120:121], v[84:85]
	v_pk_add_f32 v[122:123], v[122:123], v[86:87]
	v_mfma_f32_32x32x64_f8f6f4 v[48:63], v[42:47], v[114:119], v[48:63] cbsz:2 blgp:2
	ds_read_b128 v[42:45], v124 offset:47104
	ds_read_b64 v[46:47], v124 offset:48128
	v_exp_f32_e32 v88, v88
	v_exp_f32_e32 v89, v89
	v_exp_f32_e32 v90, v90
	v_exp_f32_e32 v91, v91
	v_pk_add_f32 v[120:121], v[120:121], v[88:89]
	v_pk_add_f32 v[122:123], v[122:123], v[90:91]
	s_setprio 2
	s_waitcnt vmcnt(4) lgkmcnt(8)
	s_barrier
	v_mfma_f32_32x32x64_f8f6f4 v[64:79], v[0:5], v[96:101], 0 cbsz:2 blgp:2
	ds_read_b128 v[0:3], v124 offset:49152
	ds_read_b64 v[4:5], v124 offset:50176
	v_exp_f32_e32 v92, v92
	v_exp_f32_e32 v93, v93
	v_exp_f32_e32 v94, v94
	v_exp_f32_e32 v95, v95
	v_pk_add_f32 v[120:121], v[120:121], v[92:93]
	v_pk_add_f32 v[122:123], v[122:123], v[94:95]
	v_mfma_f32_32x32x64_f8f6f4 v[64:79], v[6:11], v[102:107], v[64:79] cbsz:2 blgp:2
	ds_read_b128 v[6:9], v124 offset:51200
	ds_read_b64 v[10:11], v124 offset:52224
	v_exp_f32_e32 v48, v48
	v_exp_f32_e32 v49, v49
	v_exp_f32_e32 v50, v50
	v_exp_f32_e32 v51, v51
	v_pk_add_f32 v[120:121], v[120:121], v[48:49]
	v_pk_add_f32 v[122:123], v[122:123], v[50:51]
	v_mfma_f32_32x32x64_f8f6f4 v[64:79], v[12:17], v[108:113], v[64:79] cbsz:2 blgp:2
	ds_read_b128 v[12:15], v124 offset:53248
	ds_read_b64 v[16:17], v124 offset:54272
	v_exp_f32_e32 v52, v52
	v_exp_f32_e32 v53, v53
	v_exp_f32_e32 v54, v54
	v_exp_f32_e32 v55, v55
	v_pk_add_f32 v[120:121], v[120:121], v[52:53]
	v_pk_add_f32 v[122:123], v[122:123], v[54:55]
	v_mfma_f32_32x32x64_f8f6f4 v[64:79], v[18:23], v[114:119], v[64:79] cbsz:2 blgp:2
	ds_read_b128 v[18:21], v124 offset:55296
	ds_read_b64 v[22:23], v124 offset:56320
	v_exp_f32_e32 v56, v56
	v_exp_f32_e32 v57, v57
	v_exp_f32_e32 v58, v58
	v_exp_f32_e32 v59, v59
	v_pk_add_f32 v[120:121], v[120:121], v[56:57]
	v_pk_add_f32 v[122:123], v[122:123], v[58:59]
	s_waitcnt lgkmcnt(8)
	v_mfma_f32_32x32x64_f8f6f4 v[80:95], v[24:29], v[96:101], 0 cbsz:2 blgp:2
	ds_read_b128 v[24:27], v124 offset:57344
	ds_read_b64 v[28:29], v124 offset:58368
	v_exp_f32_e32 v60, v60
	v_exp_f32_e32 v61, v61
	v_exp_f32_e32 v62, v62
	v_exp_f32_e32 v63, v63
	v_pk_add_f32 v[120:121], v[120:121], v[60:61]
	v_pk_add_f32 v[122:123], v[122:123], v[62:63]
	v_mfma_f32_32x32x64_f8f6f4 v[80:95], v[30:35], v[102:107], v[80:95] cbsz:2 blgp:2
	ds_read_b128 v[30:33], v124 offset:59392
	ds_read_b64 v[34:35], v124 offset:60416
	v_exp_f32_e32 v64, v64
	v_exp_f32_e32 v65, v65
	v_exp_f32_e32 v66, v66
	v_exp_f32_e32 v67, v67
	v_pk_add_f32 v[120:121], v[120:121], v[64:65]
	v_pk_add_f32 v[122:123], v[122:123], v[66:67]
	v_mfma_f32_32x32x64_f8f6f4 v[80:95], v[36:41], v[108:113], v[80:95] cbsz:2 blgp:2
	ds_read_b128 v[36:39], v124 offset:61440
	ds_read_b64 v[40:41], v124 offset:62464
	v_exp_f32_e32 v68, v68
	v_exp_f32_e32 v69, v69
	v_exp_f32_e32 v70, v70
	v_exp_f32_e32 v71, v71
	v_pk_add_f32 v[120:121], v[120:121], v[68:69]
	v_pk_add_f32 v[122:123], v[122:123], v[70:71]
	v_mfma_f32_32x32x64_f8f6f4 v[80:95], v[42:47], v[114:119], v[80:95] cbsz:2 blgp:2
	ds_read_b128 v[42:45], v124 offset:63488
	ds_read_b64 v[46:47], v124 offset:64512
	v_exp_f32_e32 v72, v72
	v_exp_f32_e32 v73, v73
	v_exp_f32_e32 v74, v74
	v_exp_f32_e32 v75, v75
	v_pk_add_f32 v[120:121], v[120:121], v[72:73]
	v_pk_add_f32 v[122:123], v[122:123], v[74:75]
	s_waitcnt vmcnt(2) lgkmcnt(8)
	s_barrier
	v_mfma_f32_32x32x64_f8f6f4 v[48:63], v[0:5], v[96:101], 0 cbsz:2 blgp:2
	ds_read_b128 v[0:3], v124
	ds_read_b64 v[4:5], v124 offset:1024
	v_exp_f32_e32 v76, v76
	v_exp_f32_e32 v77, v77
	v_exp_f32_e32 v78, v78
	v_exp_f32_e32 v79, v79
	v_pk_add_f32 v[120:121], v[120:121], v[76:77]
	v_pk_add_f32 v[122:123], v[122:123], v[78:79]
	v_mfma_f32_32x32x64_f8f6f4 v[48:63], v[6:11], v[102:107], v[48:63] cbsz:2 blgp:2
	ds_read_b128 v[6:9], v124 offset:2048
	ds_read_b64 v[10:11], v124 offset:3072
	v_exp_f32_e32 v80, v80
	v_exp_f32_e32 v81, v81
	v_exp_f32_e32 v82, v82
	v_exp_f32_e32 v83, v83
	v_pk_add_f32 v[120:121], v[120:121], v[80:81]
	v_pk_add_f32 v[122:123], v[122:123], v[82:83]
	v_mfma_f32_32x32x64_f8f6f4 v[48:63], v[12:17], v[108:113], v[48:63] cbsz:2 blgp:2
	ds_read_b128 v[12:15], v124 offset:4096
	ds_read_b64 v[16:17], v124 offset:5120
	v_exp_f32_e32 v84, v84
	v_exp_f32_e32 v85, v85
	v_exp_f32_e32 v86, v86
	v_exp_f32_e32 v87, v87
	v_pk_add_f32 v[120:121], v[120:121], v[84:85]
	v_pk_add_f32 v[122:123], v[122:123], v[86:87]
	v_mfma_f32_32x32x64_f8f6f4 v[48:63], v[18:23], v[114:119], v[48:63] cbsz:2 blgp:2
	ds_read_b128 v[18:21], v124 offset:6144
	ds_read_b64 v[22:23], v124 offset:7168
	v_exp_f32_e32 v88, v88
	v_exp_f32_e32 v89, v89
	v_exp_f32_e32 v90, v90
	v_exp_f32_e32 v91, v91
	v_pk_add_f32 v[120:121], v[120:121], v[88:89]
	v_pk_add_f32 v[122:123], v[122:123], v[90:91]
	s_waitcnt lgkmcnt(8)
	v_mfma_f32_32x32x64_f8f6f4 v[64:79], v[24:29], v[96:101], 0 cbsz:2 blgp:2
	ds_read_b128 v[24:27], v124 offset:8192
	ds_read_b64 v[28:29], v124 offset:9216
	v_exp_f32_e32 v92, v92
	v_exp_f32_e32 v93, v93
	v_exp_f32_e32 v94, v94
	v_exp_f32_e32 v95, v95
	v_pk_add_f32 v[120:121], v[120:121], v[92:93]
	v_pk_add_f32 v[122:123], v[122:123], v[94:95]
	v_mfma_f32_32x32x64_f8f6f4 v[64:79], v[30:35], v[102:107], v[64:79] cbsz:2 blgp:2
	ds_read_b128 v[30:33], v124 offset:10240
	ds_read_b64 v[34:35], v124 offset:11264
	v_exp_f32_e32 v48, v48
	v_exp_f32_e32 v49, v49
	v_exp_f32_e32 v50, v50
	v_exp_f32_e32 v51, v51
	v_pk_add_f32 v[120:121], v[120:121], v[48:49]
	v_pk_add_f32 v[122:123], v[122:123], v[50:51]
	v_mfma_f32_32x32x64_f8f6f4 v[64:79], v[36:41], v[108:113], v[64:79] cbsz:2 blgp:2
	ds_read_b128 v[36:39], v124 offset:12288
	ds_read_b64 v[40:41], v124 offset:13312
	v_exp_f32_e32 v52, v52
	v_exp_f32_e32 v53, v53
	v_exp_f32_e32 v54, v54
	v_exp_f32_e32 v55, v55
	v_pk_add_f32 v[120:121], v[120:121], v[52:53]
	v_pk_add_f32 v[122:123], v[122:123], v[54:55]
	v_mfma_f32_32x32x64_f8f6f4 v[64:79], v[42:47], v[114:119], v[64:79] cbsz:2 blgp:2
	ds_read_b128 v[42:45], v124 offset:14336
	ds_read_b64 v[46:47], v124 offset:15360
	v_exp_f32_e32 v56, v56
	v_exp_f32_e32 v57, v57
	v_exp_f32_e32 v58, v58
	v_exp_f32_e32 v59, v59
	v_pk_add_f32 v[120:121], v[120:121], v[56:57]
	v_pk_add_f32 v[122:123], v[122:123], v[58:59]
	s_setprio 1
	s_waitcnt vmcnt(0) lgkmcnt(8)
	s_barrier
	v_mfma_f32_32x32x64_f8f6f4 v[80:95], v[0:5], v[96:101], 0 cbsz:2 blgp:2
	ds_read_b128 v[0:3], v124 offset:16384
	ds_read_b64 v[4:5], v124 offset:17408
	v_exp_f32_e32 v60, v60
	v_exp_f32_e32 v61, v61
	v_exp_f32_e32 v62, v62
	v_exp_f32_e32 v63, v63
	v_pk_add_f32 v[120:121], v[120:121], v[60:61]
	v_pk_add_f32 v[122:123], v[122:123], v[62:63]
	v_mfma_f32_32x32x64_f8f6f4 v[80:95], v[6:11], v[102:107], v[80:95] cbsz:2 blgp:2
	ds_read_b128 v[6:9], v124 offset:18432
	ds_read_b64 v[10:11], v124 offset:19456
	v_exp_f32_e32 v64, v64
	v_exp_f32_e32 v65, v65
	v_exp_f32_e32 v66, v66
	v_exp_f32_e32 v67, v67
	v_pk_add_f32 v[120:121], v[120:121], v[64:65]
	v_pk_add_f32 v[122:123], v[122:123], v[66:67]
	v_mfma_f32_32x32x64_f8f6f4 v[80:95], v[12:17], v[108:113], v[80:95] cbsz:2 blgp:2
	ds_read_b128 v[12:15], v124 offset:20480
	ds_read_b64 v[16:17], v124 offset:21504
	v_exp_f32_e32 v68, v68
	v_exp_f32_e32 v69, v69
	v_exp_f32_e32 v70, v70
	v_exp_f32_e32 v71, v71
	v_pk_add_f32 v[120:121], v[120:121], v[68:69]
	v_pk_add_f32 v[122:123], v[122:123], v[70:71]
	v_mfma_f32_32x32x64_f8f6f4 v[80:95], v[18:23], v[114:119], v[80:95] cbsz:2 blgp:2
	ds_read_b128 v[18:21], v124 offset:22528
	ds_read_b64 v[22:23], v124 offset:23552
	v_exp_f32_e32 v72, v72
	v_exp_f32_e32 v73, v73
	v_exp_f32_e32 v74, v74
	v_exp_f32_e32 v75, v75
	v_pk_add_f32 v[120:121], v[120:121], v[72:73]
	v_pk_add_f32 v[122:123], v[122:123], v[74:75]
	s_waitcnt lgkmcnt(8)
	v_mfma_f32_32x32x64_f8f6f4 v[48:63], v[24:29], v[96:101], 0 cbsz:2 blgp:2
	ds_read_b128 v[24:27], v124 offset:24576
	ds_read_b64 v[28:29], v124 offset:25600
	v_exp_f32_e32 v76, v76
	v_exp_f32_e32 v77, v77
	v_exp_f32_e32 v78, v78
	v_exp_f32_e32 v79, v79
	v_pk_add_f32 v[120:121], v[120:121], v[76:77]
	v_pk_add_f32 v[122:123], v[122:123], v[78:79]
	s_cmp_lg_u32 s8, 10
	s_cbranch_scc1 .Lmk_nosplit
	v_add_f32_e32 v127, v120, v121
	v_add_f32_e32 v125, v122, v123
	v_mov_b32_e32 v120, 0
	v_mov_b32_e32 v121, 0
	v_mov_b32_e32 v122, 0
	v_mov_b32_e32 v123, 0
	v_add_f32_e32 v127, v127, v125
.Lmk_nosplit:
	v_mfma_f32_32x32x64_f8f6f4 v[48:63], v[30:35], v[102:107], v[48:63] cbsz:2 blgp:2
	ds_read_b128 v[30:33], v124 offset:26624
	ds_read_b64 v[34:35], v124 offset:27648
	v_exp_f32_e32 v80, v80
	v_exp_f32_e32 v81, v81
	v_exp_f32_e32 v82, v82
	v_exp_f32_e32 v83, v83
	v_pk_add_f32 v[120:121], v[120:121], v[80:81]
	v_pk_add_f32 v[122:123], v[122:123], v[82:83]
	v_mfma_f32_32x32x64_f8f6f4 v[48:63], v[36:41], v[108:113], v[48:63] cbsz:2 blgp:2
	ds_read_b128 v[36:39], v124 offset:28672
	ds_read_b64 v[40:41], v124 offset:29696
	v_exp_f32_e32 v84, v84
	v_exp_f32_e32 v85, v85
	v_exp_f32_e32 v86, v86
	v_exp_f32_e32 v87, v87
	v_pk_add_f32 v[120:121], v[120:121], v[84:85]
	v_pk_add_f32 v[122:123], v[122:123], v[86:87]
	v_mfma_f32_32x32x64_f8f6f4 v[48:63], v[42:47], v[114:119], v[48:63] cbsz:2 blgp:2
	ds_read_b128 v[42:45], v124 offset:30720
	ds_read_b64 v[46:47], v124 offset:31744
	v_exp_f32_e32 v88, v88
	v_exp_f32_e32 v89, v89
	v_exp_f32_e32 v90, v90
	v_exp_f32_e32 v91, v91
	v_pk_add_f32 v[120:121], v[120:121], v[88:89]
	v_pk_add_f32 v[122:123], v[122:123], v[90:91]
	s_setprio 0
	s_waitcnt lgkmcnt(8)
	v_mfma_f32_32x32x64_f8f6f4 v[64:79], v[0:5], v[96:101], 0 cbsz:2 blgp:2
	v_exp_f32_e32 v92, v92
	v_exp_f32_e32 v93, v93
	v_exp_f32_e32 v94, v94
	v_exp_f32_e32 v95, v95
	v_pk_add_f32 v[120:121], v[120:121], v[92:93]
	v_pk_add_f32 v[122:123], v[122:123], v[94:95]
	v_mfma_f32_32x32x64_f8f6f4 v[64:79], v[6:11], v[102:107], v[64:79] cbsz:2 blgp:2
	v_exp_f32_e32 v48, v48
	v_exp_f32_e32 v49, v49
	v_exp_f32_e32 v50, v50
	v_exp_f32_e32 v51, v51
	v_pk_add_f32 v[120:121], v[120:121], v[48:49]
	v_pk_add_f32 v[122:123], v[122:123], v[50:51]
	v_mfma_f32_32x32x64_f8f6f4 v[64:79], v[12:17], v[108:113], v[64:79] cbsz:2 blgp:2
	v_exp_f32_e32 v52, v52
	v_exp_f32_e32 v53, v53
	v_exp_f32_e32 v54, v54
	v_exp_f32_e32 v55, v55
	v_pk_add_f32 v[120:121], v[120:121], v[52:53]
	v_pk_add_f32 v[122:123], v[122:123], v[54:55]
	v_mfma_f32_32x32x64_f8f6f4 v[64:79], v[18:23], v[114:119], v[64:79] cbsz:2 blgp:2
	v_exp_f32_e32 v56, v56
	v_exp_f32_e32 v57, v57
	v_exp_f32_e32 v58, v58
	v_exp_f32_e32 v59, v59
	v_pk_add_f32 v[120:121], v[120:121], v[56:57]
	v_pk_add_f32 v[122:123], v[122:123], v[58:59]
	s_waitcnt lgkmcnt(0)
	v_mfma_f32_32x32x64_f8f6f4 v[80:95], v[24:29], v[96:101], 0 cbsz:2 blgp:2
	v_exp_f32_e32 v60, v60
	v_exp_f32_e32 v61, v61
	v_exp_f32_e32 v62, v62
	v_exp_f32_e32 v63, v63
	v_pk_add_f32 v[120:121], v[120:121], v[60:61]
	v_pk_add_f32 v[122:123], v[122:123], v[62:63]
	v_mfma_f32_32x32x64_f8f6f4 v[80:95], v[30:35], v[102:107], v[80:95] cbsz:2 blgp:2
	v_exp_f32_e32 v64, v64
	v_exp_f32_e32 v65, v65
	v_exp_f32_e32 v66, v66
	v_exp_f32_e32 v67, v67
	v_pk_add_f32 v[120:121], v[120:121], v[64:65]
	v_pk_add_f32 v[122:123], v[122:123], v[66:67]
	v_mfma_f32_32x32x64_f8f6f4 v[80:95], v[36:41], v[108:113], v[80:95] cbsz:2 blgp:2
	v_exp_f32_e32 v68, v68
	v_exp_f32_e32 v69, v69
	v_exp_f32_e32 v70, v70
	v_exp_f32_e32 v71, v71
	v_pk_add_f32 v[120:121], v[120:121], v[68:69]
	v_pk_add_f32 v[122:123], v[122:123], v[70:71]
	v_mfma_f32_32x32x64_f8f6f4 v[80:95], v[42:47], v[114:119], v[80:95] cbsz:2 blgp:2
	v_exp_f32_e32 v72, v72
	v_exp_f32_e32 v73, v73
	v_exp_f32_e32 v74, v74
	v_exp_f32_e32 v75, v75
	v_pk_add_f32 v[120:121], v[120:121], v[72:73]
	v_pk_add_f32 v[122:123], v[122:123], v[74:75]
	v_exp_f32_e32 v76, v76
	v_exp_f32_e32 v77, v77
	v_exp_f32_e32 v78, v78
	v_exp_f32_e32 v79, v79
	v_pk_add_f32 v[120:121], v[120:121], v[76:77]
	v_pk_add_f32 v[122:123], v[122:123], v[78:79]
	s_nop 1
	v_exp_f32_e32 v80, v80
	v_exp_f32_e32 v81, v81
	v_exp_f32_e32 v82, v82
	v_exp_f32_e32 v83, v83
	v_pk_add_f32 v[120:121], v[120:121], v[80:81]
	v_pk_add_f32 v[122:123], v[122:123], v[82:83]
	v_exp_f32_e32 v84, v84
	v_exp_f32_e32 v85, v85
	v_exp_f32_e32 v86, v86
	v_exp_f32_e32 v87, v87
	v_pk_add_f32 v[120:121], v[120:121], v[84:85]
	v_pk_add_f32 v[122:123], v[122:123], v[86:87]
	v_exp_f32_e32 v88, v88
	v_exp_f32_e32 v89, v89
	v_exp_f32_e32 v90, v90
	v_exp_f32_e32 v91, v91
	v_pk_add_f32 v[120:121], v[120:121], v[88:89]
	v_pk_add_f32 v[122:123], v[122:123], v[90:91]
	v_exp_f32_e32 v92, v92
	v_exp_f32_e32 v93, v93
	v_exp_f32_e32 v94, v94
	v_exp_f32_e32 v95, v95
	v_pk_add_f32 v[120:121], v[120:121], v[92:93]
	v_pk_add_f32 v[122:123], v[122:123], v[94:95]
	v_add_f32_e32 v120, v120, v121
	v_add_f32_e32 v122, v122, v123
	v_lshrrev_b32_e32 v126, 2, v124
	v_add_f32_e32 v120, v120, v122
	v_xor_b32_e32 v125, 0x80, v126
	s_load_dwordx4 s[4:7], s[0:1], 0x8
	ds_bpermute_b32 v122, v125, v120
	ds_bpermute_b32 v123, v125, v127
	s_lshl_b32 s14, s14, 7
	v_add_u32_e32 v126, s14, v126
	v_cmp_gt_u32_e32 vcc, 0x200, v124
	s_and_saveexec_b64 s[16:17], vcc
	s_cbranch_execz .Lmk_end
	s_waitcnt lgkmcnt(0)
	v_add_f32_e32 v120, v120, v122
	v_add_f32_e32 v127, v127, v123
	s_cmp_lt_u32 s8, 10
	s_cbranch_scc1 .Lmk_pos_only
	s_cmp_eq_u32 s8, 10
	s_cbranch_scc0 .Lmk_neg_only
	global_atomic_add_f32 v126, v127, s[4:5]
.Lmk_neg_only:
	global_atomic_add_f32 v126, v120, s[6:7]
	s_endpgm
.Lmk_pos_only:
	global_atomic_add_f32 v126, v120, s[4:5]

	.amdhsa_kernel _Z11main_kernelPKcPfS1_
		.amdhsa_group_segment_fixed_size 65536
		.amdhsa_private_segment_fixed_size 0
		.amdhsa_kernarg_size 24
		.amdhsa_user_sgpr_count 2
		.amdhsa_user_sgpr_dispatch_ptr 0
		.amdhsa_user_sgpr_queue_ptr 0
		.amdhsa_user_sgpr_kernarg_segment_ptr 1
		.amdhsa_user_sgpr_dispatch_id 0
		.amdhsa_user_sgpr_kernarg_preload_length 0
		.amdhsa_user_sgpr_kernarg_preload_offset 0
		.amdhsa_user_sgpr_private_segment_size 0
		.amdhsa_uses_dynamic_stack 0
		.amdhsa_enable_private_segment 0
		.amdhsa_system_sgpr_workgroup_id_x 1
		.amdhsa_system_sgpr_workgroup_id_y 0
		.amdhsa_system_sgpr_workgroup_id_z 0
		.amdhsa_system_sgpr_workgroup_info 0
		.amdhsa_system_vgpr_workitem_id 0
		.amdhsa_next_free_vgpr 128
		.amdhsa_next_free_sgpr 96
		.amdhsa_accum_offset 128
		.amdhsa_reserve_vcc 1
		.amdhsa_float_round_mode_32 0
		.amdhsa_float_round_mode_16_64 0
		.amdhsa_float_denorm_mode_32 3
		.amdhsa_float_denorm_mode_16_64 3
		.amdhsa_dx10_clamp 1
		.amdhsa_ieee_mode 1
		.amdhsa_fp16_overflow 0
		.amdhsa_tg_split 0
		.amdhsa_exception_fp_ieee_invalid_op 0
		.amdhsa_exception_fp_denorm_src 0
		.amdhsa_exception_fp_ieee_div_zero 0
		.amdhsa_exception_fp_ieee_overflow 0
		.amdhsa_exception_fp_ieee_underflow 0
		.amdhsa_exception_fp_ieee_inexact 0
		.amdhsa_exception_int_div_zero 0
	.end_amdhsa_kernel

amdhsa.kernels:
  - .agpr_count:     0
    .args:
      - .actual_access:  read_only
        .address_space:  global
        .offset:         0
        .size:           8
        .value_kind:     global_buffer
      - .actual_access:  read_only
        .address_space:  global
        .offset:         8
        .size:           8
        .value_kind:     global_buffer
      - .actual_access:  read_only
        .address_space:  global
        .offset:         16
        .size:           8
        .value_kind:     global_buffer
      - .actual_access:  write_only
        .address_space:  global
        .offset:         24
        .size:           8
        .value_kind:     global_buffer
      - .actual_access:  write_only
        .address_space:  global
        .offset:         32
        .size:           8
        .value_kind:     global_buffer
      - .actual_access:  write_only
        .address_space:  global
        .offset:         40
        .size:           8
        .value_kind:     global_buffer
      - .actual_access:  write_only
        .address_space:  global
        .offset:         48
        .size:           8
        .value_kind:     global_buffer
      - .actual_access:  write_only
        .address_space:  global
        .offset:         56
        .size:           8
        .value_kind:     global_buffer
    .group_segment_fixed_size: 23040
    .kernarg_segment_align: 8
    .kernarg_segment_size: 64
    .language:       OpenCL C
    .language_version:
      - 2
      - 0
    .max_flat_workgroup_size: 1024
    .name:           _Z11prep_kernelPKfS0_S0_PcPfS2_S2_S2_
    .private_segment_fixed_size: 0
    .sgpr_count:     22
    .sgpr_spill_count: 0
    .symbol:         _Z11prep_kernelPKfS0_S0_PcPfS2_S2_S2_.kd
    .uniform_work_group_size: 1
    .uses_dynamic_stack: false
    .vgpr_count:     46
    .vgpr_spill_count: 0
    .wavefront_size: 64
  - .agpr_count:     0
    .args:
      - .address_space:  global
        .offset:         0
        .size:           8
        .value_kind:     global_buffer
      - .address_space:  global
        .offset:         8
        .size:           8
        .value_kind:     global_buffer
      - .address_space:  global
        .offset:         16
        .size:           8
        .value_kind:     global_buffer
    .group_segment_fixed_size: 65536
    .kernarg_segment_align: 8
    .kernarg_segment_size: 24
    .language:       OpenCL C
    .language_version:
      - 2
      - 0
    .max_flat_workgroup_size: 512
    .name:           _Z11main_kernelPKcPfS1_
    .private_segment_fixed_size: 0
    .sgpr_count:     34
    .sgpr_spill_count: 0
    .symbol:         _Z11main_kernelPKcPfS1_.kd
    .uniform_work_group_size: 1
    .uses_dynamic_stack: false
    .vgpr_count:     128
    .vgpr_spill_count: 0
    .wavefront_size: 64
  - .agpr_count:     0
    .args:
      - .actual_access:  read_only
        .address_space:  global
        .offset:         0
        .size:           8
        .value_kind:     global_buffer
      - .actual_access:  read_only
        .address_space:  global
        .offset:         8
        .size:           8
        .value_kind:     global_buffer
      - .actual_access:  read_only
        .address_space:  global
        .offset:         16
        .size:           8
        .value_kind:     global_buffer
      - .actual_access:  read_only
        .address_space:  global
        .offset:         24
        .size:           8
        .value_kind:     global_buffer
      - .address_space:  global
        .offset:         32
        .size:           8
        .value_kind:     global_buffer
    .group_segment_fixed_size: 2064
    .kernarg_segment_align: 8
    .kernarg_segment_size: 40
    .language:       OpenCL C
    .language_version:
      - 2
      - 0
    .max_flat_workgroup_size: 256
    .name:           _Z12final_kernelPKfS0_S0_S0_Pf
    .private_segment_fixed_size: 0
    .sgpr_count:     18
    .sgpr_spill_count: 0
    .symbol:         _Z12final_kernelPKfS0_S0_S0_Pf.kd
    .uniform_work_group_size: 1
    .uses_dynamic_stack: false
    .vgpr_count:     35
    .vgpr_spill_count: 0
    .wavefront_size: 64
